# e4n
# speedup vs baseline: 1.0265x; 1.0265x over previous
.LBB6_7:
	v_mov_b32_e32 v232, v216
	v_mov_b32_e32 v233, v217
	v_mov_b32_e32 v234, v218
	v_mov_b32_e32 v235, v219
	v_mov_b32_e32 v236, v220
	v_mov_b32_e32 v237, v221
	v_mov_b32_e32 v238, v222
	v_mov_b32_e32 v239, v223
	v_mov_b32_e32 v240, v224
	v_mov_b32_e32 v241, v225
	v_mov_b32_e32 v242, v226
	v_mov_b32_e32 v243, v227
	v_mov_b32_e32 v244, v228
	v_mov_b32_e32 v245, v229
	v_mov_b32_e32 v246, v230
	v_mov_b32_e32 v247, v231
	s_waitcnt vmcnt(10)
	v_mfma_f32_32x32x64_f8f6f4 v[0:15], v[56:63], v[88:95], 0
	s_or_b32 s0, s14, s6
	ds_read_b128 v[16:19], v162
	ds_read_b128 v[20:23], v162 offset:32
	ds_read_b128 v[24:27], v162 offset:64
	ds_read_b128 v[28:31], v162 offset:96
	s_or_b32 s2, s0, 1
	s_add_i32 s1, s0, 2
	s_lshl_b64 s[12:13], s[2:3], 13
	s_and_b64 s[14:15], s[10:11], exec
	v_lshl_add_u64 v[112:113], v[152:153], 0, s[12:13]
	s_cselect_b32 s12, s1, s0
	s_lshl_b32 s1, s0, 11
	v_or_b32_e32 v100, s1, v158
	global_load_dwordx4 v[96:99], v[112:113], off
	v_add_co_u32_e32 v132, vcc, s5, v112
	s_lshl_b32 s9, s2, 11
	s_nop 0
	v_addc_co_u32_e32 v133, vcc, 0, v113, vcc
	s_waitcnt vmcnt(9)
	v_mfma_f32_32x32x64_f8f6f4 v[0:15], v[40:47], v[72:79], v[0:15]
	v_or_b32_e32 v214, s9, v158
	s_mov_b32 s13, s3
	s_lshl_b64 s[12:13], s[12:13], 13
	s_lshl_b64 s[16:17], s[2:3], 11
	s_mov_b32 s14, 2
	s_waitcnt vmcnt(7)
	v_mfma_f32_32x32x64_f8f6f4 v[0:15], v[48:55], v[80:87], v[0:15]
	s_waitcnt vmcnt(5)
	v_mfma_f32_32x32x64_f8f6f4 v[0:15], v[32:39], v[64:71], v[0:15]
	s_waitcnt lgkmcnt(3)
	s_nop 15
	s_nop 2
	v_pk_fma_f32 v[0:1], v[0:1], s[4:5], v[16:17] op_sel_hi:[1,0,1]
	v_pk_fma_f32 v[2:3], v[2:3], s[4:5], v[18:19] op_sel_hi:[1,0,1]
	s_waitcnt lgkmcnt(2)
	v_pk_fma_f32 v[4:5], v[4:5], s[4:5], v[20:21] op_sel_hi:[1,0,1]
	v_pk_fma_f32 v[6:7], v[6:7], s[4:5], v[22:23] op_sel_hi:[1,0,1]
	s_waitcnt lgkmcnt(1)
	v_pk_fma_f32 v[8:9], v[8:9], s[4:5], v[24:25] op_sel_hi:[1,0,1]
	v_pk_fma_f32 v[10:11], v[10:11], s[4:5], v[26:27] op_sel_hi:[1,0,1]
	s_waitcnt lgkmcnt(0)
	v_pk_fma_f32 v[12:13], v[12:13], s[4:5], v[28:29] op_sel_hi:[1,0,1]
	v_pk_fma_f32 v[14:15], v[14:15], s[4:5], v[30:31] op_sel_hi:[1,0,1]
	v_cvt_pk_bf16_f32 v0, v0, v1
	v_cvt_pk_bf16_f32 v1, v2, v3
	v_cvt_pk_bf16_f32 v2, v4, v5
	v_cvt_pk_bf16_f32 v3, v6, v7
	v_cvt_pk_bf16_f32 v4, v8, v9
	v_cvt_pk_bf16_f32 v5, v10, v11
	v_cvt_pk_bf16_f32 v6, v12, v13
	v_cvt_pk_bf16_f32 v7, v14, v15
	ds_write_b128 v100, v[0:3]
	ds_write_b128 v100, v[4:7] offset:1024
	ds_read_b128 v[0:3], v165
	ds_read_b128 v[4:7], v167
	s_waitcnt lgkmcnt(0)
	v_mfma_f32_32x32x64_f8f6f4 v[0:15], v[88:95], v[0:7], 0
	global_load_dwordx4 v[100:103], v[112:113], off offset:1024
	global_load_dwordx4 v[104:107], v[112:113], off offset:2048
	ds_read_b128 v[114:117], v168
	ds_read_b128 v[118:121], v169
	global_load_dwordx4 v[108:111], v[112:113], off offset:3072
	s_waitcnt lgkmcnt(0)
	v_mfma_f32_32x32x64_f8f6f4 v[0:15], v[72:79], v[114:121], v[0:15]
	global_load_dwordx4 v[112:115], v[132:133], off
	ds_read_b128 v[116:119], v170
	ds_read_b128 v[120:123], v171
	s_waitcnt lgkmcnt(0)
	v_mfma_f32_32x32x64_f8f6f4 v[0:15], v[80:87], v[116:123], v[0:15]
	global_load_dwordx4 v[116:119], v[132:133], off offset:1024
	global_load_dwordx4 v[120:123], v[132:133], off offset:2048
	ds_read_b128 v[124:127], v172
	ds_read_b128 v[128:131], v173
	s_waitcnt lgkmcnt(0)
	v_mfma_f32_32x32x64_f8f6f4 v[0:15], v[64:71], v[124:131], v[0:15]
	global_load_dwordx4 v[124:127], v[132:133], off offset:3072
	ds_read_b32 v128, v155 offset:256
	v_add_u32_e32 v129, s1, v166
	s_mov_b32 s1, s3
	s_lshl_b64 s[0:1], s[0:1], 11
	s_waitcnt lgkmcnt(0)
	s_nop 13
	v_pk_fma_f32 v[0:1], v[0:1], s[4:5], v[128:129] op_sel_hi:[1,0,0]
	s_waitcnt vmcnt(6)
	v_mfma_f32_32x32x64_f8f6f4 v[16:31], v[56:63], v[96:103], 0
	v_fma_f32 v2, v2, s4, v128
	v_fma_f32 v3, v3, s4, v128
	v_fma_f32 v4, v4, s4, v128
	v_fma_f32 v5, v5, s4, v128
	v_fma_f32 v6, v6, s4, v128
	v_fma_f32 v7, v7, s4, v128
	v_fma_f32 v8, v8, s4, v128
	v_fma_f32 v9, v9, s4, v128
	v_fma_f32 v10, v10, s4, v128
	v_fma_f32 v11, v11, s4, v128
	v_fma_f32 v12, v12, s4, v128
	v_fma_f32 v13, v13, s4, v128
	v_fma_f32 v14, v14, s4, v128
	v_fma_f32 v15, v15, s4, v128
	v_cvt_pk_bf16_f32 v0, v0, v1
	v_cvt_pk_bf16_f32 v1, v2, v3
	v_cvt_pk_bf16_f32 v2, v4, v5
	v_cvt_pk_bf16_f32 v3, v6, v7
	v_cvt_pk_bf16_f32 v4, v8, v9
	v_cvt_pk_bf16_f32 v5, v10, v11
	v_cvt_pk_bf16_f32 v6, v12, v13
	v_cvt_pk_bf16_f32 v7, v14, v15
	s_waitcnt vmcnt(4)
	v_mfma_f32_32x32x64_f8f6f4 v[16:31], v[40:47], v[104:111], v[16:31]
	ds_write_b128 v129, v[0:3]
	ds_write_b128 v129, v[4:7] offset:1024
	ds_read_b128 v[0:3], v174
	ds_read_b128 v[4:7], v175
	ds_read_b128 v[182:185], v176
	ds_read_b128 v[186:189], v177
	ds_read_b128 v[190:193], v178
	ds_read_b128 v[194:197], v179
	ds_read_b128 v[128:131], v180
	ds_read_b128 v[132:135], v181
	ds_read_b128 v[148:151], v163
	ds_read_b128 v[144:147], v163 offset:32
	ds_read_b128 v[140:143], v163 offset:64
	ds_read_b128 v[136:139], v163 offset:96
	ds_read_b128 v[198:201], v162
	ds_read_b128 v[202:205], v162 offset:32
	ds_read_b128 v[206:209], v162 offset:64
	ds_read_b128 v[210:213], v162 offset:96
	s_waitcnt vmcnt(2)
	v_mfma_f32_32x32x64_f8f6f4 v[16:31], v[48:55], v[112:119], v[16:31]
	s_waitcnt vmcnt(0)
	v_mfma_f32_32x32x64_f8f6f4 v[16:31], v[32:39], v[120:127], v[16:31]
	s_waitcnt lgkmcnt(14)
	v_mfma_f32_32x32x64_f8f6f4 v[0:15], v[0:7], v[88:95], 0
	s_waitcnt lgkmcnt(3)
	s_nop 15
	s_nop 0
	v_fma_f32 v16, v16, s4, v198
	v_fma_f32 v17, v17, s4, v199
	v_fma_f32 v18, v18, s4, v200
	v_fma_f32 v19, v19, s4, v201
	s_waitcnt lgkmcnt(2)
	v_fma_f32 v20, v20, s4, v202
	v_fma_f32 v21, v21, s4, v203
	v_fma_f32 v22, v22, s4, v204
	v_fma_f32 v23, v23, s4, v205
	s_waitcnt lgkmcnt(1)
	v_fma_f32 v24, v24, s4, v206
	v_fma_f32 v25, v25, s4, v207
	v_pk_fma_f32 v[26:27], v[26:27], s[4:5], v[208:209] op_sel_hi:[1,0,1]
	s_waitcnt lgkmcnt(0)
	v_pk_fma_f32 v[28:29], v[28:29], s[4:5], v[210:211] op_sel_hi:[1,0,1]
	v_pk_fma_f32 v[30:31], v[30:31], s[4:5], v[212:213] op_sel_hi:[1,0,1]
	v_cvt_pk_bf16_f32 v16, v16, v17
	v_cvt_pk_bf16_f32 v17, v18, v19
	v_cvt_pk_bf16_f32 v18, v20, v21
	v_cvt_pk_bf16_f32 v19, v22, v23
	v_cvt_pk_bf16_f32 v20, v24, v25
	v_cvt_pk_bf16_f32 v21, v26, v27
	v_cvt_pk_bf16_f32 v22, v28, v29
	v_cvt_pk_bf16_f32 v23, v30, v31
	ds_write_b128 v214, v[16:19]
	ds_write_b128 v214, v[20:23] offset:1024
	ds_read_b128 v[16:19], v165
	ds_read_b128 v[20:23], v167
	ds_read_b128 v[88:91], v168
	ds_read_b32 v198, v155 offset:256
	s_waitcnt lgkmcnt(2)
	v_mfma_f32_32x32x64_f8f6f4 v[16:31], v[96:103], v[16:23], 0
	v_mfma_f32_32x32x64_f8f6f4 v[0:15], v[182:189], v[72:79], v[0:15]
	ds_read_b128 v[92:95], v169
	ds_read_b128 v[72:75], v170
	ds_read_b128 v[76:79], v171
	ds_read_b128 v[182:185], v172
	s_waitcnt lgkmcnt(3)
	v_mfma_f32_32x32x64_f8f6f4 v[16:31], v[104:111], v[88:95], v[16:31]
	v_mfma_f32_32x32x64_f8f6f4 v[0:15], v[190:197], v[80:87], v[0:15]
	v_lshl_add_u64 v[190:191], v[160:161], 0, s[0:1]
	v_add_u32_e32 v194, s9, v166
	v_lshl_add_u64 v[192:193], v[160:161], 0, s[16:17]
	s_waitcnt lgkmcnt(1)
	v_mfma_f32_32x32x64_f8f6f4 v[16:31], v[112:119], v[72:79], v[16:31]
	v_cndmask_b32_e64 v72, 0, 1, s[10:11]
	v_cmp_ne_u32_e32 vcc, 1, v72
	s_mov_b64 s[10:11], 0
	s_and_b64 vcc, exec, vcc
	v_mfma_f32_32x32x64_f8f6f4 v[0:15], v[128:135], v[64:71], v[0:15]
	v_lshl_add_u64 v[64:65], v[152:153], 0, s[12:13]
	global_load_dwordx4 v[88:91], v[64:65], off
	global_load_dwordx4 v[92:95], v[64:65], off offset:1024
	ds_read_b128 v[186:189], v173
	v_add_co_u32_e64 v68, s[0:1], s5, v64
	s_nop 14
	v_pk_fma_f32 v[0:1], v[0:1], s[4:5], v[148:149] op_sel_hi:[1,0,1]
	s_waitcnt lgkmcnt(0)
	v_mfma_f32_32x32x64_f8f6f4 v[16:31], v[120:127], v[182:189], v[16:31]
	v_addc_co_u32_e64 v69, s[0:1], 0, v65, s[0:1]
	global_load_dwordx4 v[72:75], v[64:65], off offset:2048
	global_load_dwordx4 v[76:79], v[64:65], off offset:3072
	global_load_dwordx4 v[80:83], v[68:69], off
	global_load_dwordx4 v[84:87], v[68:69], off offset:1024
	s_nop 0
	global_load_dwordx4 v[64:67], v[68:69], off offset:2048
	s_nop 0
	global_load_dwordx4 v[68:71], v[68:69], off offset:3072
	v_fma_f32 v2, v2, s4, v150
	v_fma_f32 v3, v3, s4, v151
	v_fma_f32 v4, v4, s4, v144
	v_fma_f32 v5, v5, s4, v145
	v_fma_f32 v128, v6, s4, v146
	v_fma_f32 v129, v7, s4, v147
	v_pk_mul_f32 v[146:147], v[0:1], s[8:9] op_sel_hi:[1,0]
	v_pk_mul_f32 v[148:149], v[2:3], s[8:9] op_sel_hi:[1,0]
	v_pk_mul_f32 v[150:151], v[4:5], s[8:9] op_sel_hi:[1,0]
	v_pk_fma_f32 v[130:131], v[8:9], s[4:5], v[140:141] op_sel_hi:[1,0,1]
	v_pk_fma_f32 v[132:133], v[10:11], s[4:5], v[142:143] op_sel_hi:[1,0,1]
	v_pk_fma_f32 v[134:135], v[12:13], s[4:5], v[136:137] op_sel_hi:[1,0,1]
	v_pk_fma_f32 v[144:145], v[14:15], s[4:5], v[138:139] op_sel_hi:[1,0,1]
	v_pk_fma_f32 v[0:1], v[16:17], s[4:5], v[198:199] op_sel_hi:[1,0,0]
	v_pk_fma_f32 v[2:3], v[18:19], s[4:5], v[198:199] op_sel_hi:[1,0,0]
	v_pk_fma_f32 v[4:5], v[20:21], s[4:5], v[198:199] op_sel_hi:[1,0,0]
	v_pk_fma_f32 v[6:7], v[22:23], s[4:5], v[198:199] op_sel_hi:[1,0,0]
	v_pk_fma_f32 v[8:9], v[24:25], s[4:5], v[198:199] op_sel_hi:[1,0,0]
	v_pk_fma_f32 v[10:11], v[26:27], s[4:5], v[198:199] op_sel_hi:[1,0,0]
	v_pk_fma_f32 v[12:13], v[28:29], s[4:5], v[198:199] op_sel_hi:[1,0,0]
	v_pk_fma_f32 v[14:15], v[30:31], s[4:5], v[198:199] op_sel_hi:[1,0,0]
	v_cvt_pk_bf16_f32 v0, v0, v1
	v_cvt_pk_bf16_f32 v1, v2, v3
	v_cvt_pk_bf16_f32 v2, v4, v5
	v_cvt_pk_bf16_f32 v3, v6, v7
	v_cvt_pk_bf16_f32 v4, v8, v9
	v_cvt_pk_bf16_f32 v5, v10, v11
	v_cvt_pk_bf16_f32 v6, v12, v13
	v_cvt_pk_bf16_f32 v7, v14, v15
	ds_write_b128 v194, v[0:3]
	ds_write_b128 v194, v[4:7] offset:1024
	ds_read_b128 v[136:139], v174
	ds_read_b128 v[140:143], v175
	s_waitcnt lgkmcnt(0)
	v_mfma_f32_32x32x64_f8f6f4 v[0:15], v[136:143], v[96:103], 0
	v_mul_f32_e64 v20, v128, s8
	v_mul_f32_e64 v21, v129, s8
	v_mul_f32_e64 v22, v130, s8
	v_mul_f32_e64 v23, v131, s8
	v_mul_f32_e64 v24, v132, s8
	v_mul_f32_e64 v25, v133, s8
	v_mul_f32_e64 v26, v134, s8
	v_mul_f32_e64 v27, v135, s8
	ds_read_b128 v[128:131], v176
	ds_read_b128 v[132:135], v177
	v_mul_f32_e64 v28, v144, s8
	v_mul_f32_e64 v29, v145, s8
	v_cvt_pk_bf16_f32 v16, v146, v147
	v_cvt_pk_bf16_f32 v17, v148, v149
	v_cvt_pk_bf16_f32 v18, v150, v151
	v_cvt_pk_bf16_f32 v19, v20, v21
	v_cvt_pk_bf16_f32 v20, v22, v23
	v_cvt_pk_bf16_f32 v21, v24, v25
	v_cvt_pk_bf16_f32 v22, v26, v27
	v_cvt_pk_bf16_f32 v23, v28, v29
	s_waitcnt lgkmcnt(0)
	v_mfma_f32_32x32x64_f8f6f4 v[0:15], v[128:135], v[104:111], v[0:15]
	ds_read_b128 v[104:107], v178
	ds_read_b128 v[108:111], v179
	v_mov_b32_e32 v216, v16
	v_mov_b32_e32 v217, v17
	v_mov_b32_e32 v218, v18
	v_mov_b32_e32 v219, v19
	v_mov_b32_e32 v220, v20
	v_mov_b32_e32 v221, v21
	v_mov_b32_e32 v222, v22
	v_mov_b32_e32 v223, v23
	s_waitcnt lgkmcnt(0)
	v_mfma_f32_32x32x64_f8f6f4 v[0:15], v[104:111], v[112:119], v[0:15]
	ds_read_b128 v[96:99], v180
	ds_read_b128 v[100:103], v181
	ds_read_b128 v[148:151], v163
	ds_read_b128 v[144:147], v163 offset:32
	ds_read_b128 v[116:119], v163 offset:64
	ds_read_b128 v[112:115], v163 offset:96
	s_waitcnt lgkmcnt(4)
	v_mfma_f32_32x32x64_f8f6f4 v[0:15], v[96:103], v[120:127], v[0:15]
	s_waitcnt lgkmcnt(3)
	s_nop 15
	s_nop 2
	v_pk_fma_f32 v[0:1], v[0:1], s[4:5], v[148:149] op_sel_hi:[1,0,1]
	v_pk_fma_f32 v[2:3], v[2:3], s[4:5], v[150:151] op_sel_hi:[1,0,1]
	s_waitcnt lgkmcnt(2)
	v_pk_fma_f32 v[4:5], v[4:5], s[4:5], v[144:145] op_sel_hi:[1,0,1]
	v_pk_fma_f32 v[6:7], v[6:7], s[4:5], v[146:147] op_sel_hi:[1,0,1]
	s_waitcnt lgkmcnt(1)
	v_pk_fma_f32 v[8:9], v[8:9], s[4:5], v[116:117] op_sel_hi:[1,0,1]
	v_pk_fma_f32 v[10:11], v[10:11], s[4:5], v[118:119] op_sel_hi:[1,0,1]
	s_waitcnt lgkmcnt(0)
	v_pk_fma_f32 v[12:13], v[12:13], s[4:5], v[112:113] op_sel_hi:[1,0,1]
	v_pk_fma_f32 v[14:15], v[14:15], s[4:5], v[114:115] op_sel_hi:[1,0,1]
	v_pk_mul_f32 v[0:1], v[0:1], s[8:9] op_sel_hi:[1,0]
	v_pk_mul_f32 v[2:3], v[2:3], s[8:9] op_sel_hi:[1,0]
	v_pk_mul_f32 v[4:5], v[4:5], s[8:9] op_sel_hi:[1,0]
	v_pk_mul_f32 v[6:7], v[6:7], s[8:9] op_sel_hi:[1,0]
	v_pk_mul_f32 v[8:9], v[8:9], s[8:9] op_sel_hi:[1,0]
	v_pk_mul_f32 v[10:11], v[10:11], s[8:9] op_sel_hi:[1,0]
	v_pk_mul_f32 v[12:13], v[12:13], s[8:9] op_sel_hi:[1,0]
	v_pk_mul_f32 v[14:15], v[14:15], s[8:9] op_sel_hi:[1,0]
	v_cvt_pk_bf16_f32 v0, v0, v1
	v_cvt_pk_bf16_f32 v1, v2, v3
	v_cvt_pk_bf16_f32 v2, v4, v5
	v_cvt_pk_bf16_f32 v3, v6, v7
	v_cvt_pk_bf16_f32 v4, v8, v9
	v_cvt_pk_bf16_f32 v5, v10, v11
	v_cvt_pk_bf16_f32 v6, v12, v13
	v_cvt_pk_bf16_f32 v7, v14, v15
	v_mov_b32_e32 v224, v0
	v_mov_b32_e32 v225, v1
	v_mov_b32_e32 v226, v2
	v_mov_b32_e32 v227, v3
	v_mov_b32_e32 v228, v4
	v_mov_b32_e32 v229, v5
	v_mov_b32_e32 v230, v6
	v_mov_b32_e32 v231, v7
	s_cbranch_vccz .LBB6_7
	s_cmpk_gt_u32 s29, 0xbf
	v_cmp_gt_u32_e32 vcc, 2, v157
	s_cbranch_scc1 .LBB6_26
	v_mov_b32_e32 v0, 0x25c00
	v_lshl_add_u32 v0, v157, 8, v0
	v_lshlrev_b32_e32 v1, 3, v164
	v_mov_b32_e32 v20, 0
	v_add_u32_e32 v0, v0, v1
	v_mov_b32_e32 v28, 0
	v_mov_b32_e32 v29, 0
	v_mov_b32_e32 v30, 0
	v_mov_b32_e32 v31, 0
	v_mov_b32_e32 v24, 0
	v_mov_b32_e32 v25, 0
	v_mov_b32_e32 v26, 0
	v_mov_b32_e32 v27, 0
	s_and_saveexec_b64 s[0:1], vcc
	s_cbranch_execz .LBB6_11
	ds_read2_b64 v[24:27], v0 offset1:2
	ds_read2_b64 v[28:31], v0 offset0:4 offset1:6

.LBB6_26:
	s_lshl_b64 s[0:1], s[6:7], 11
	v_lshl_add_u64 v[0:1], v[160:161], 0, s[0:1]
	s_or_b32 s0, s6, 1
	s_mov_b32 s1, 0
	s_waitcnt vmcnt(0)
	s_waitcnt lgkmcnt(0)
	s_barrier
	v_mov_b32_e32 v112, v232
	v_mov_b32_e32 v113, v233
	v_mov_b32_e32 v114, v234
	v_mov_b32_e32 v115, v235
	s_lshl_b64 s[2:3], s[0:1], 11
	v_lshl_add_u64 v[2:3], v[160:161], 0, s[2:3]
	v_mov_b32_e32 v116, v240
	v_mov_b32_e32 v117, v241
	v_mov_b32_e32 v118, v242
	v_mov_b32_e32 v119, v243
	v_mov_b32_e32 v120, v236
	v_mov_b32_e32 v121, v237
	v_mov_b32_e32 v122, v238
	v_mov_b32_e32 v123, v239
	v_mov_b32_e32 v124, v244
	v_mov_b32_e32 v125, v245
	v_mov_b32_e32 v126, v246
	v_mov_b32_e32 v127, v247
	v_add_co_u32_e32 v0, vcc, 0x10000, v160
	s_mov_b32 s2, 0x3f803f80
	s_nop 0
	v_addc_co_u32_e32 v1, vcc, 0, v161, vcc
	global_load_dwordx4 v[104:107], v[0:1], off
	global_load_dwordx4 v[100:103], v[0:1], off offset:1024
	ds_read_b128 v[136:139], v158
	ds_read_b128 v[132:135], v158 offset:1024
	v_mov_b32_e32 v0, 0
	s_mov_b32 s3, s2
	v_mov_b32_e32 v1, v0
	v_mov_b32_e32 v2, v0
	v_mov_b32_e32 v3, v0
	v_mov_b32_e32 v4, v0
	v_mov_b32_e32 v5, v0
	v_mov_b32_e32 v6, v0
	v_mov_b32_e32 v7, v0
	v_mov_b32_e32 v8, v0
	v_mov_b32_e32 v9, v0
	v_mov_b32_e32 v10, v0
	v_mov_b32_e32 v11, v0
	v_mov_b32_e32 v12, v0
	v_mov_b32_e32 v13, v0
	v_mov_b32_e32 v14, v0
	v_mov_b32_e32 v15, v0
	v_mov_b32_e32 v16, v0
	v_mov_b32_e32 v17, v0
	v_mov_b32_e32 v18, v0
	v_mov_b32_e32 v19, v0
	v_mov_b32_e32 v20, v0
	v_mov_b32_e32 v21, v0
	v_mov_b32_e32 v22, v0
	v_mov_b32_e32 v23, v0
	v_mov_b32_e32 v24, v0
	v_mov_b32_e32 v25, v0
	v_mov_b32_e32 v26, v0
	v_mov_b32_e32 v27, v0
	v_mov_b32_e32 v28, v0
	v_mov_b32_e32 v29, v0
	v_mov_b32_e32 v30, v0
	v_mov_b32_e32 v31, v0
	v_mov_b64_e32 v[96:97], s[2:3]
	v_mov_b32_e32 v144, v0
	v_mov_b32_e32 v145, v0
	v_mov_b32_e32 v146, v0
	v_mov_b32_e32 v147, v0
	v_mov_b32_e32 v140, v0
	v_mov_b32_e32 v141, v0
	v_mov_b32_e32 v142, v0
	v_mov_b32_e32 v143, v0
	s_waitcnt vmcnt(5) lgkmcnt(1)
	v_mfma_f32_32x32x16_bf16 v[48:63], v[136:139], v[112:115], 0
	s_waitcnt vmcnt(4)
	v_mfma_f32_32x32x16_bf16 v[32:47], v[136:139], v[116:119], 0
	s_waitcnt vmcnt(3) lgkmcnt(0)
	v_mfma_f32_32x32x16_bf16 v[48:63], v[132:135], v[120:123], v[48:63]
	s_waitcnt vmcnt(2)
	v_mfma_f32_32x32x16_bf16 v[32:47], v[132:135], v[124:127], v[32:47]
	v_mov_b32_e32 v180, v0
	v_mov_b32_e32 v181, v0
	v_mov_b32_e32 v182, v0
	v_mov_b32_e32 v183, v0
	v_mov_b32_e32 v184, v0
	v_mov_b32_e32 v185, v0
	v_mov_b32_e32 v186, v0
	v_mov_b32_e32 v187, v0
	v_mov_b32_e32 v76, v0
	v_mov_b32_e32 v77, v0
	v_mov_b32_e32 v78, v0
	v_mov_b32_e32 v79, v0
	v_mov_b32_e32 v168, v0
	v_mov_b32_e32 v169, v0
	v_mov_b32_e32 v170, v0
	v_mov_b32_e32 v171, v0
	v_mov_b32_e32 v248, v0
	v_mov_b32_e32 v249, v0
	v_mov_b32_e32 v250, v0
	v_mov_b32_e32 v251, v0
	ds_read_b128 v[196:199], v158 offset:2048
	ds_read_b128 v[108:111], v158 offset:3072
	s_nop 0
.Lmy_attn_loop1:
	v_add_u32_e32 v252, s1, v158
	v_add_u32_e32 v253, 0x10800, v252
	s_waitcnt lgkmcnt(0)
	v_mfma_f32_32x32x16_bf16 v[80:95], v[196:199], v[112:115], 0
	ds_read_b128 v[128:131], v253 offset:0
	ds_read_b128 v[148:151], v253 offset:1024
	v_cvt_pk_bf16_f32 v186, v76, v77
	v_cvt_pk_bf16_f32 v187, v78, v79
	v_exp_f32_e32 v48, v48
	v_exp_f32_e32 v49, v49
	v_exp_f32_e32 v50, v50
	v_exp_f32_e32 v51, v51
	v_mfma_f32_4x4x4_16b_bf16 v[140:143], v[96:97], v[180:181], v[140:143]
	v_mfma_f32_32x32x16_bf16 v[80:95], v[108:111], v[120:123], v[80:95]
	v_exp_f32_e32 v52, v52
	v_exp_f32_e32 v53, v53
	v_exp_f32_e32 v54, v54
	v_exp_f32_e32 v55, v55
	v_cvt_pk_bf16_f32 v172, v48, v49
	v_cvt_pk_bf16_f32 v173, v50, v51
	v_mfma_f32_4x4x4_16b_bf16 v[140:143], v[96:97], v[182:183], v[140:143]
	v_mfma_f32_32x32x16_bf16 v[0:15], v[168:171], v[180:183], v[0:15]
	v_exp_f32_e32 v56, v56
	v_exp_f32_e32 v57, v57
	v_exp_f32_e32 v58, v58
	v_exp_f32_e32 v59, v59
	v_cvt_pk_bf16_f32 v174, v52, v53
	v_cvt_pk_bf16_f32 v175, v54, v55
	v_mfma_f32_4x4x4_16b_bf16 v[140:143], v[96:97], v[184:185], v[140:143]
	v_mfma_f32_32x32x16_bf16 v[0:15], v[248:251], v[184:187], v[0:15]
	v_exp_f32_e32 v60, v60
	v_exp_f32_e32 v61, v61
	v_exp_f32_e32 v62, v62
	v_exp_f32_e32 v63, v63
	v_cvt_pk_bf16_f32 v176, v56, v57
	v_cvt_pk_bf16_f32 v177, v58, v59
	v_mfma_f32_4x4x4_16b_bf16 v[140:143], v[96:97], v[186:187], v[140:143]
	v_mfma_f32_32x32x16_bf16 v[64:79], v[196:199], v[116:119], 0
	ds_read_b128 v[188:191], v252 offset:4096
	ds_read_b128 v[192:195], v252 offset:5120
	v_cvt_pk_bf16_f32 v178, v60, v61
	v_cvt_pk_bf16_f32 v179, v62, v63
	v_exp_f32_e32 v32, v32
	v_exp_f32_e32 v33, v33
	v_exp_f32_e32 v34, v34
	v_exp_f32_e32 v35, v35
	v_mfma_f32_4x4x4_16b_bf16 v[144:147], v[96:97], v[172:173], v[144:147]
	v_mfma_f32_32x32x16_bf16 v[64:79], v[108:111], v[124:127], v[64:79]
	v_exp_f32_e32 v36, v36
	v_exp_f32_e32 v37, v37
	v_exp_f32_e32 v38, v38
	v_exp_f32_e32 v39, v39
	v_cvt_pk_bf16_f32 v180, v32, v33
	v_cvt_pk_bf16_f32 v181, v34, v35
	v_mfma_f32_4x4x4_16b_bf16 v[144:147], v[96:97], v[174:175], v[144:147]
	s_waitcnt lgkmcnt(2)
	v_mfma_f32_32x32x16_bf16 v[16:31], v[128:131], v[172:175], v[16:31]
	v_exp_f32_e32 v40, v40
	v_exp_f32_e32 v41, v41
	v_exp_f32_e32 v42, v42
	v_exp_f32_e32 v43, v43
	v_cvt_pk_bf16_f32 v182, v36, v37
	v_cvt_pk_bf16_f32 v183, v38, v39
	v_mfma_f32_4x4x4_16b_bf16 v[144:147], v[96:97], v[176:177], v[144:147]
	v_mfma_f32_32x32x16_bf16 v[16:31], v[148:151], v[176:179], v[16:31]
	v_exp_f32_e32 v44, v44
	v_exp_f32_e32 v45, v45
	v_exp_f32_e32 v46, v46
	v_exp_f32_e32 v47, v47
	v_cvt_pk_bf16_f32 v184, v40, v41
	v_cvt_pk_bf16_f32 v185, v42, v43
	v_mfma_f32_4x4x4_16b_bf16 v[144:147], v[96:97], v[178:179], v[144:147]
	s_waitcnt lgkmcnt(0)
	v_mfma_f32_32x32x16_bf16 v[48:63], v[188:191], v[112:115], 0
	ds_read_b128 v[168:171], v253 offset:2048
	ds_read_b128 v[248:251], v253 offset:3072
	v_cvt_pk_bf16_f32 v186, v44, v45
	v_cvt_pk_bf16_f32 v187, v46, v47
	v_exp_f32_e32 v80, v80
	v_exp_f32_e32 v81, v81
	v_exp_f32_e32 v82, v82
	v_exp_f32_e32 v83, v83
	v_mfma_f32_4x4x4_16b_bf16 v[140:143], v[96:97], v[180:181], v[140:143]
	v_mfma_f32_32x32x16_bf16 v[48:63], v[192:195], v[120:123], v[48:63]
	v_exp_f32_e32 v84, v84
	v_exp_f32_e32 v85, v85
	v_exp_f32_e32 v86, v86
	v_exp_f32_e32 v87, v87
	v_cvt_pk_bf16_f32 v172, v80, v81
	v_cvt_pk_bf16_f32 v173, v82, v83
	v_mfma_f32_4x4x4_16b_bf16 v[140:143], v[96:97], v[182:183], v[140:143]
	v_mfma_f32_32x32x16_bf16 v[0:15], v[128:131], v[180:183], v[0:15]
	v_exp_f32_e32 v88, v88
	v_exp_f32_e32 v89, v89
	v_exp_f32_e32 v90, v90
	v_exp_f32_e32 v91, v91
	v_cvt_pk_bf16_f32 v174, v84, v85
	v_cvt_pk_bf16_f32 v175, v86, v87
	v_mfma_f32_4x4x4_16b_bf16 v[140:143], v[96:97], v[184:185], v[140:143]
	v_mfma_f32_32x32x16_bf16 v[0:15], v[148:151], v[184:187], v[0:15]
	v_exp_f32_e32 v92, v92
	v_exp_f32_e32 v93, v93
	v_exp_f32_e32 v94, v94
	v_exp_f32_e32 v95, v95
	v_cvt_pk_bf16_f32 v176, v88, v89
	v_cvt_pk_bf16_f32 v177, v90, v91
	v_mfma_f32_4x4x4_16b_bf16 v[140:143], v[96:97], v[186:187], v[140:143]
	v_mfma_f32_32x32x16_bf16 v[32:47], v[188:191], v[116:119], 0
	ds_read_b128 v[196:199], v252 offset:6144
	ds_read_b128 v[108:111], v252 offset:7168
	v_cvt_pk_bf16_f32 v178, v92, v93
	v_cvt_pk_bf16_f32 v179, v94, v95
	v_exp_f32_e32 v64, v64
	v_exp_f32_e32 v65, v65
	v_exp_f32_e32 v66, v66
	v_exp_f32_e32 v67, v67
	v_mfma_f32_4x4x4_16b_bf16 v[144:147], v[96:97], v[172:173], v[144:147]
	v_mfma_f32_32x32x16_bf16 v[32:47], v[192:195], v[124:127], v[32:47]
	v_exp_f32_e32 v68, v68
	v_exp_f32_e32 v69, v69
	v_exp_f32_e32 v70, v70
	v_exp_f32_e32 v71, v71
	v_cvt_pk_bf16_f32 v180, v64, v65
	v_cvt_pk_bf16_f32 v181, v66, v67
	v_mfma_f32_4x4x4_16b_bf16 v[144:147], v[96:97], v[174:175], v[144:147]
	s_waitcnt lgkmcnt(2)
	v_mfma_f32_32x32x16_bf16 v[16:31], v[168:171], v[172:175], v[16:31]
	v_exp_f32_e32 v72, v72
	v_exp_f32_e32 v73, v73
	v_exp_f32_e32 v74, v74
	v_exp_f32_e32 v75, v75
	v_cvt_pk_bf16_f32 v182, v68, v69
	v_cvt_pk_bf16_f32 v183, v70, v71
	v_mfma_f32_4x4x4_16b_bf16 v[144:147], v[96:97], v[176:177], v[144:147]
	v_mfma_f32_32x32x16_bf16 v[16:31], v[248:251], v[176:179], v[16:31]
	v_exp_f32_e32 v76, v76
	v_exp_f32_e32 v77, v77
	v_exp_f32_e32 v78, v78
	v_exp_f32_e32 v79, v79
	v_cvt_pk_bf16_f32 v184, v72, v73
	v_cvt_pk_bf16_f32 v185, v74, v75
	v_mfma_f32_4x4x4_16b_bf16 v[144:147], v[96:97], v[178:179], v[144:147]
	s_addk_i32 s1, 0x1000
	s_cmp_lg_u32 s1, 0x10000
	s_cbranch_scc1 .Lmy_attn_loop1
	v_cvt_pk_bf16_f32 v186, v76, v77
	v_cvt_pk_bf16_f32 v187, v78, v79
	v_mfma_f32_4x4x4_16b_bf16 v[140:143], v[96:97], v[180:181], v[140:143]
	v_mfma_f32_32x32x16_bf16 v[0:15], v[168:171], v[180:183], v[0:15]
	s_nop 0
	v_mfma_f32_4x4x4_16b_bf16 v[140:143], v[96:97], v[182:183], v[140:143]
	v_mfma_f32_32x32x16_bf16 v[0:15], v[248:251], v[184:187], v[0:15]
	s_nop 0
	v_mfma_f32_4x4x4_16b_bf16 v[140:143], v[96:97], v[184:185], v[140:143]
	s_nop 1
	v_mfma_f32_4x4x4_16b_bf16 v[140:143], v[96:97], v[186:187], v[140:143]
	v_mov_b32_e32 v34, 0x3f80
	v_cmp_gt_u32_e64 s[0:1], 32, v154
	v_or_b32_e32 v36, 0x20c00, v158
	s_mov_b32 s2, 0x3f803f80
	v_cndmask_b32_e64 v96, 0, v34, s[0:1]
	v_or_b32_e32 v34, 0x20800, v158
	ds_read_b128 v[108:111], v34
	ds_read_b128 v[128:131], v36
	v_exp_f32_e32 v34, v48
	v_exp_f32_e32 v35, v49
	s_mov_b32 s3, s2
	v_mov_b64_e32 v[52:53], s[2:3]
	v_exp_f32_e32 v32, v32
	v_exp_f32_e32 v33, v33
	v_mov_b32_e32 v97, 0
	v_cndmask_b32_e64 v34, 0, v34, s[0:1]
	v_cndmask_b32_e64 v35, 0, v35, s[0:1]
	v_cvt_pk_bf16_f32 v34, v34, v35
	v_mov_b32_e32 v35, v97
	v_mov_b32_e32 v36, v97
	v_mov_b32_e32 v37, v97
	s_mov_b32 s8, 0
	v_cndmask_b32_e64 v32, 0, v32, s[0:1]
	v_cndmask_b32_e64 v33, 0, v33, s[0:1]
	s_waitcnt lgkmcnt(1)
	v_mfma_f32_32x32x16_bf16 v[16:31], v[108:111], v[34:37], v[16:31]
	s_mov_b32 s9, s8
	v_cvt_pk_bf16_f32 v46, v32, v33
	v_mov_b64_e32 v[50:51], s[8:9]
	v_mov_b32_e32 v32, v46
	v_mov_b32_e32 v33, v97
	v_mov_b32_e32 v47, v97
	v_mov_b32_e32 v48, v97
	v_mfma_f32_4x4x4_16b_bf16 v[34:37], v[52:53], v[34:35], v[144:147]
	v_mov_b32_e32 v49, v97
	s_mov_b32 s10, s8
	v_mfma_f32_4x4x4_16b_bf16 v[38:41], v[52:53], v[50:51], v[34:37]
	s_mov_b32 s11, s8
	v_mfma_f32_4x4x4_16b_bf16 v[32:35], v[52:53], v[32:33], v[140:143]
	v_mov_b64_e32 v[44:45], s[10:11]
	v_mfma_f32_32x32x16_bf16 v[0:15], v[108:111], v[46:49], v[0:15]
	v_mov_b64_e32 v[42:43], s[8:9]
	s_mov_b32 s7, 0x7149f2ca
	s_mov_b32 s4, 0xda24260
	v_mov_b32_e32 v98, v97
	v_mov_b32_e32 v99, v97
	v_mfma_f32_4x4x4_16b_bf16 v[32:35], v[52:53], v[50:51], v[32:35]
	s_waitcnt lgkmcnt(0)
	v_mfma_f32_32x32x16_bf16 v[16:31], v[128:131], v[42:45], v[16:31]
	s_nop 2
	v_mbcnt_lo_u32_b32 v33, -1, 0
	v_mbcnt_hi_u32_b32 v33, -1, v33
	v_and_b32_e32 v35, 64, v33
	v_xor_b32_e32 v34, 32, v33
	v_add_u32_e32 v35, 64, v35
	v_cmp_lt_i32_e32 vcc, v34, v35
	v_mfma_f32_32x32x16_bf16 v[0:15], v[128:131], v[42:45], v[0:15]
	s_nop 0
	v_cndmask_b32_e32 v33, v33, v34, vcc
	v_lshlrev_b32_e32 v165, 2, v33
	ds_bpermute_b32 v35, v165, v38
	ds_bpermute_b32 v34, v165, v32
	v_mov_b32_e32 v33, v38
	s_waitcnt lgkmcnt(0)
	v_pk_add_f32 v[34:35], v[32:33], v[34:35]
	s_nop 0
	v_cmp_ngt_f32_e32 vcc, s7, v35
	v_cmp_nlt_f32_e64 s[2:3], s4, v34
	v_cmp_nlt_f32_e64 s[4:5], s4, v35
	s_or_b64 s[4:5], s[4:5], vcc
	v_cmp_ngt_f32_e32 vcc, s7, v34
	s_or_b64 s[2:3], s[2:3], vcc
	s_or_b64 vcc, s[4:5], s[2:3]
	s_cbranch_vccnz .LBB6_40

.LBB6_34:
	s_or_b64 exec, exec, s[4:5]
	s_or_b32 s26, s6, 2
	s_mov_b32 s27, 0
	s_lshl_b64 s[4:5], s[26:27], 11
	s_waitcnt lgkmcnt(0)
	v_lshl_add_u64 v[0:1], v[160:161], 0, s[4:5]
	s_or_b32 s4, s6, 3
	s_mov_b32 s5, s27
	v_mov_b32_e32 v100, v216
	v_mov_b32_e32 v101, v217
	v_mov_b32_e32 v102, v218
	v_mov_b32_e32 v103, v219
	s_lshl_b64 s[4:5], s[4:5], 11
	v_lshl_add_u64 v[2:3], v[160:161], 0, s[4:5]
	v_mov_b32_e32 v104, v224
	v_mov_b32_e32 v105, v225
	v_mov_b32_e32 v106, v226
	v_mov_b32_e32 v107, v227
	v_mov_b32_e32 v108, v220
	v_mov_b32_e32 v109, v221
	v_mov_b32_e32 v110, v222
	v_mov_b32_e32 v111, v223
	v_mov_b32_e32 v112, v228
	v_mov_b32_e32 v113, v229
	v_mov_b32_e32 v114, v230
	v_mov_b32_e32 v115, v231
	ds_read_b128 v[132:135], v158
	ds_read_b128 v[128:131], v158 offset:1024
	s_mov_b32 s4, 0x3f803f80
	v_mov_b32_e32 v136, 0
	s_mov_b32 s5, s4
	v_mov_b32_e32 v137, v136
	v_mov_b32_e32 v138, v136
	v_mov_b32_e32 v139, v136
	v_mov_b32_e32 v140, v136
	v_mov_b32_e32 v141, v136
	v_mov_b32_e32 v142, v136
	v_mov_b32_e32 v143, v136
	v_mov_b32_e32 v0, v136
	v_mov_b32_e32 v1, v136
	v_mov_b32_e32 v2, v136
	v_mov_b32_e32 v3, v136
	v_mov_b32_e32 v4, v136
	v_mov_b32_e32 v5, v136
	v_mov_b32_e32 v6, v136
	v_mov_b32_e32 v7, v136
	v_mov_b32_e32 v8, v136
	v_mov_b32_e32 v9, v136
	v_mov_b32_e32 v10, v136
	v_mov_b32_e32 v11, v136
	v_mov_b32_e32 v12, v136
	v_mov_b32_e32 v13, v136
	v_mov_b32_e32 v14, v136
	v_mov_b32_e32 v15, v136
	v_mov_b32_e32 v16, v136
	v_mov_b32_e32 v17, v136
	v_mov_b32_e32 v18, v136
	v_mov_b32_e32 v19, v136
	v_mov_b32_e32 v20, v136
	v_mov_b32_e32 v21, v136
	v_mov_b32_e32 v22, v136
	v_mov_b32_e32 v23, v136
	v_mov_b64_e32 v[116:117], s[4:5]
	v_mov_b32_e32 v24, v136
	v_mov_b32_e32 v25, v136
	v_mov_b32_e32 v26, v136
	v_mov_b32_e32 v27, v136
	v_mov_b32_e32 v28, v136
	v_mov_b32_e32 v29, v136
	v_mov_b32_e32 v30, v136
	v_mov_b32_e32 v31, v136
	s_waitcnt vmcnt(3) lgkmcnt(1)
	v_mfma_f32_32x32x16_bf16 v[48:63], v[132:135], v[100:103], 0
	s_waitcnt vmcnt(2)
	v_mfma_f32_32x32x16_bf16 v[32:47], v[132:135], v[104:107], 0
	s_waitcnt vmcnt(1) lgkmcnt(0)
	v_mfma_f32_32x32x16_bf16 v[48:63], v[128:131], v[108:111], v[48:63]
	s_waitcnt vmcnt(0)
	v_mfma_f32_32x32x16_bf16 v[32:47], v[128:131], v[112:115], v[32:47]
	v_mov_b32_e32 v180, v136
	v_mov_b32_e32 v181, v136
	v_mov_b32_e32 v182, v136
	v_mov_b32_e32 v183, v136
	v_mov_b32_e32 v184, v136
	v_mov_b32_e32 v185, v136
	v_mov_b32_e32 v186, v136
	v_mov_b32_e32 v187, v136
	v_mov_b32_e32 v76, v136
	v_mov_b32_e32 v77, v136
	v_mov_b32_e32 v78, v136
	v_mov_b32_e32 v79, v136
	v_mov_b32_e32 v240, v136
	v_mov_b32_e32 v241, v136
	v_mov_b32_e32 v242, v136
	v_mov_b32_e32 v243, v136
	v_mov_b32_e32 v244, v136
	v_mov_b32_e32 v245, v136
	v_mov_b32_e32 v246, v136
	v_mov_b32_e32 v247, v136
	ds_read_b128 v[224:227], v158 offset:2048
	ds_read_b128 v[228:231], v158 offset:3072
	s_nop 0
.Lmy_attn_loop2:
	v_add_u32_e32 v248, s27, v158
	v_add_u32_e32 v249, 0x10800, v248
	s_waitcnt lgkmcnt(0)
	v_mfma_f32_32x32x16_bf16 v[80:95], v[224:227], v[100:103], 0
	ds_read_b128 v[232:235], v249 offset:0
	ds_read_b128 v[236:239], v249 offset:1024
	v_cvt_pk_bf16_f32 v186, v76, v77
	v_cvt_pk_bf16_f32 v187, v78, v79
	v_exp_f32_e32 v48, v48
	v_exp_f32_e32 v49, v49
	v_exp_f32_e32 v50, v50
	v_exp_f32_e32 v51, v51
	v_mfma_f32_4x4x4_16b_bf16 v[136:139], v[116:117], v[180:181], v[136:139]
	v_mfma_f32_32x32x16_bf16 v[80:95], v[228:231], v[108:111], v[80:95]
	v_exp_f32_e32 v52, v52
	v_exp_f32_e32 v53, v53
	v_exp_f32_e32 v54, v54
	v_exp_f32_e32 v55, v55
	v_cvt_pk_bf16_f32 v172, v48, v49
	v_cvt_pk_bf16_f32 v173, v50, v51
	v_mfma_f32_4x4x4_16b_bf16 v[136:139], v[116:117], v[182:183], v[136:139]
	v_mfma_f32_32x32x16_bf16 v[0:15], v[240:243], v[180:183], v[0:15]
	v_exp_f32_e32 v56, v56
	v_exp_f32_e32 v57, v57
	v_exp_f32_e32 v58, v58
	v_exp_f32_e32 v59, v59
	v_cvt_pk_bf16_f32 v174, v52, v53
	v_cvt_pk_bf16_f32 v175, v54, v55
	v_mfma_f32_4x4x4_16b_bf16 v[136:139], v[116:117], v[184:185], v[136:139]
	v_mfma_f32_32x32x16_bf16 v[0:15], v[244:247], v[184:187], v[0:15]
	v_exp_f32_e32 v60, v60
	v_exp_f32_e32 v61, v61
	v_exp_f32_e32 v62, v62
	v_exp_f32_e32 v63, v63
	v_cvt_pk_bf16_f32 v176, v56, v57
	v_cvt_pk_bf16_f32 v177, v58, v59
	v_mfma_f32_4x4x4_16b_bf16 v[136:139], v[116:117], v[186:187], v[136:139]
	v_mfma_f32_32x32x16_bf16 v[64:79], v[224:227], v[104:107], 0
	ds_read_b128 v[216:219], v248 offset:4096
	ds_read_b128 v[220:223], v248 offset:5120
	v_cvt_pk_bf16_f32 v178, v60, v61
	v_cvt_pk_bf16_f32 v179, v62, v63
	v_exp_f32_e32 v32, v32
	v_exp_f32_e32 v33, v33
	v_exp_f32_e32 v34, v34
	v_exp_f32_e32 v35, v35
	v_mfma_f32_4x4x4_16b_bf16 v[140:143], v[116:117], v[172:173], v[140:143]
	v_mfma_f32_32x32x16_bf16 v[64:79], v[228:231], v[112:115], v[64:79]
	v_exp_f32_e32 v36, v36
	v_exp_f32_e32 v37, v37
	v_exp_f32_e32 v38, v38
	v_exp_f32_e32 v39, v39
	v_cvt_pk_bf16_f32 v180, v32, v33
	v_cvt_pk_bf16_f32 v181, v34, v35
	v_mfma_f32_4x4x4_16b_bf16 v[140:143], v[116:117], v[174:175], v[140:143]
	s_waitcnt lgkmcnt(2)
	v_mfma_f32_32x32x16_bf16 v[16:31], v[232:235], v[172:175], v[16:31]
	v_exp_f32_e32 v40, v40
	v_exp_f32_e32 v41, v41
	v_exp_f32_e32 v42, v42
	v_exp_f32_e32 v43, v43
	v_cvt_pk_bf16_f32 v182, v36, v37
	v_cvt_pk_bf16_f32 v183, v38, v39
	v_mfma_f32_4x4x4_16b_bf16 v[140:143], v[116:117], v[176:177], v[140:143]
	v_mfma_f32_32x32x16_bf16 v[16:31], v[236:239], v[176:179], v[16:31]
	v_exp_f32_e32 v44, v44
	v_exp_f32_e32 v45, v45
	v_exp_f32_e32 v46, v46
	v_exp_f32_e32 v47, v47
	v_cvt_pk_bf16_f32 v184, v40, v41
	v_cvt_pk_bf16_f32 v185, v42, v43
	v_mfma_f32_4x4x4_16b_bf16 v[140:143], v[116:117], v[178:179], v[140:143]
	s_waitcnt lgkmcnt(0)
	v_mfma_f32_32x32x16_bf16 v[48:63], v[216:219], v[100:103], 0
	ds_read_b128 v[240:243], v249 offset:2048
	ds_read_b128 v[244:247], v249 offset:3072
	v_cvt_pk_bf16_f32 v186, v44, v45
	v_cvt_pk_bf16_f32 v187, v46, v47
	v_exp_f32_e32 v80, v80
	v_exp_f32_e32 v81, v81
	v_exp_f32_e32 v82, v82
	v_exp_f32_e32 v83, v83
	v_mfma_f32_4x4x4_16b_bf16 v[136:139], v[116:117], v[180:181], v[136:139]
	v_mfma_f32_32x32x16_bf16 v[48:63], v[220:223], v[108:111], v[48:63]
	v_exp_f32_e32 v84, v84
	v_exp_f32_e32 v85, v85
	v_exp_f32_e32 v86, v86
	v_exp_f32_e32 v87, v87
	v_cvt_pk_bf16_f32 v172, v80, v81
	v_cvt_pk_bf16_f32 v173, v82, v83
	v_mfma_f32_4x4x4_16b_bf16 v[136:139], v[116:117], v[182:183], v[136:139]
	v_mfma_f32_32x32x16_bf16 v[0:15], v[232:235], v[180:183], v[0:15]
	v_exp_f32_e32 v88, v88
	v_exp_f32_e32 v89, v89
	v_exp_f32_e32 v90, v90
	v_exp_f32_e32 v91, v91
	v_cvt_pk_bf16_f32 v174, v84, v85
	v_cvt_pk_bf16_f32 v175, v86, v87
	v_mfma_f32_4x4x4_16b_bf16 v[136:139], v[116:117], v[184:185], v[136:139]
	v_mfma_f32_32x32x16_bf16 v[0:15], v[236:239], v[184:187], v[0:15]
	v_exp_f32_e32 v92, v92
	v_exp_f32_e32 v93, v93
	v_exp_f32_e32 v94, v94
	v_exp_f32_e32 v95, v95
	v_cvt_pk_bf16_f32 v176, v88, v89
	v_cvt_pk_bf16_f32 v177, v90, v91
	v_mfma_f32_4x4x4_16b_bf16 v[136:139], v[116:117], v[186:187], v[136:139]
	v_mfma_f32_32x32x16_bf16 v[32:47], v[216:219], v[104:107], 0
	ds_read_b128 v[224:227], v248 offset:6144
	ds_read_b128 v[228:231], v248 offset:7168
	v_cvt_pk_bf16_f32 v178, v92, v93
	v_cvt_pk_bf16_f32 v179, v94, v95
	v_exp_f32_e32 v64, v64
	v_exp_f32_e32 v65, v65
	v_exp_f32_e32 v66, v66
	v_exp_f32_e32 v67, v67
	v_mfma_f32_4x4x4_16b_bf16 v[140:143], v[116:117], v[172:173], v[140:143]
	v_mfma_f32_32x32x16_bf16 v[32:47], v[220:223], v[112:115], v[32:47]
	v_exp_f32_e32 v68, v68
	v_exp_f32_e32 v69, v69
	v_exp_f32_e32 v70, v70
	v_exp_f32_e32 v71, v71
	v_cvt_pk_bf16_f32 v180, v64, v65
	v_cvt_pk_bf16_f32 v181, v66, v67
	v_mfma_f32_4x4x4_16b_bf16 v[140:143], v[116:117], v[174:175], v[140:143]
	s_waitcnt lgkmcnt(2)
	v_mfma_f32_32x32x16_bf16 v[16:31], v[240:243], v[172:175], v[16:31]
	v_exp_f32_e32 v72, v72
	v_exp_f32_e32 v73, v73
	v_exp_f32_e32 v74, v74
	v_exp_f32_e32 v75, v75
	v_cvt_pk_bf16_f32 v182, v68, v69
	v_cvt_pk_bf16_f32 v183, v70, v71
	v_mfma_f32_4x4x4_16b_bf16 v[140:143], v[116:117], v[176:177], v[140:143]
	v_mfma_f32_32x32x16_bf16 v[16:31], v[244:247], v[176:179], v[16:31]
	v_exp_f32_e32 v76, v76
	v_exp_f32_e32 v77, v77
	v_exp_f32_e32 v78, v78
	v_exp_f32_e32 v79, v79
	v_cvt_pk_bf16_f32 v184, v72, v73
	v_cvt_pk_bf16_f32 v185, v74, v75
	v_mfma_f32_4x4x4_16b_bf16 v[140:143], v[116:117], v[178:179], v[140:143]
	s_addk_i32 s27, 0x1000
	s_cmp_lg_u32 s27, 0x10000
	s_cbranch_scc1 .Lmy_attn_loop2
	v_cvt_pk_bf16_f32 v186, v76, v77
	v_cvt_pk_bf16_f32 v187, v78, v79
	v_mfma_f32_4x4x4_16b_bf16 v[136:139], v[116:117], v[180:181], v[136:139]
	v_mfma_f32_32x32x16_bf16 v[0:15], v[240:243], v[180:183], v[0:15]
	s_nop 0
	v_mfma_f32_4x4x4_16b_bf16 v[136:139], v[116:117], v[182:183], v[136:139]
	v_mfma_f32_32x32x16_bf16 v[0:15], v[244:247], v[184:187], v[0:15]
	s_nop 0
	v_mfma_f32_4x4x4_16b_bf16 v[136:139], v[116:117], v[184:185], v[136:139]
	s_nop 1
	v_mfma_f32_4x4x4_16b_bf16 v[136:139], v[116:117], v[186:187], v[136:139]
	v_or_b32_e32 v34, 0x20800, v158
	ds_read_b128 v[116:119], v34
	v_or_b32_e32 v36, 0x20c00, v158
	s_mov_b32 s4, 0x3f803f80
	v_exp_f32_e32 v35, v49
	ds_read_b128 v[120:123], v36
	v_exp_f32_e32 v34, v48
	s_mov_b32 s5, s4
	v_mov_b64_e32 v[46:47], s[4:5]
	v_exp_f32_e32 v38, v32
	v_exp_f32_e32 v39, v33
	v_cndmask_b32_e64 v34, 0, v34, s[0:1]
	v_cndmask_b32_e64 v35, 0, v35, s[0:1]
	v_mov_b32_e32 v125, 0
	v_cvt_pk_bf16_f32 v124, v34, v35
	v_mov_b32_e32 v126, v125
	v_mov_b32_e32 v127, v125
	v_cndmask_b32_e64 v38, 0, v38, s[0:1]
	v_cndmask_b32_e64 v39, 0, v39, s[0:1]
	s_waitcnt lgkmcnt(1)
	v_mfma_f32_32x32x16_bf16 v[16:31], v[116:119], v[124:127], v[16:31]
	s_mov_b32 s8, 0
	s_mov_b32 s9, s8
	v_mov_b64_e32 v[36:37], s[8:9]
	s_mov_b32 s10, s8
	s_mov_b32 s11, s8
	v_mov_b64_e32 v[44:45], s[10:11]
	v_mov_b64_e32 v[42:43], s[8:9]
	v_mfma_f32_4x4x4_16b_bf16 v[32:35], v[46:47], v[124:125], v[140:143]
	v_cvt_pk_bf16_f32 v124, v38, v39
	s_waitcnt lgkmcnt(0)
	v_mfma_f32_32x32x16_bf16 v[16:31], v[120:123], v[42:45], v[16:31]
	s_mov_b32 s9, 0x7149f2ca
	s_mov_b32 s6, 0xda24260
	v_mfma_f32_32x32x16_bf16 v[0:15], v[116:119], v[124:127], v[0:15]
	v_mfma_f32_4x4x4_16b_bf16 v[38:41], v[46:47], v[36:37], v[32:35]
	v_mfma_f32_4x4x4_16b_bf16 v[32:35], v[46:47], v[124:125], v[136:139]
	v_mfma_f32_32x32x16_bf16 v[0:15], v[120:123], v[42:45], v[0:15]
	s_nop 0
	v_mfma_f32_4x4x4_16b_bf16 v[32:35], v[46:47], v[36:37], v[32:35]
	s_nop 4
	ds_bpermute_b32 v35, v165, v38
	ds_bpermute_b32 v34, v165, v32
	v_mov_b32_e32 v33, v38
	s_waitcnt lgkmcnt(0)
	v_pk_add_f32 v[34:35], v[32:33], v[34:35]
	s_nop 0
	v_cmp_ngt_f32_e32 vcc, s9, v35
	v_cmp_nlt_f32_e64 s[4:5], s6, v34
	v_cmp_nlt_f32_e64 s[6:7], s6, v35
	s_or_b64 s[6:7], s[6:7], vcc
	v_cmp_ngt_f32_e32 vcc, s9, v34
	s_or_b64 s[4:5], s[4:5], vcc
	s_or_b64 vcc, s[6:7], s[4:5]
	s_cbranch_vccnz .LBB6_64

	.amdhsa_kernel _Z9attn_mfmaPKtS0_PKfS2_PtS3_S3_
		.amdhsa_group_segment_fixed_size 155648
		.amdhsa_private_segment_fixed_size 0
		.amdhsa_kernarg_size 56
		.amdhsa_user_sgpr_count 2
		.amdhsa_user_sgpr_dispatch_ptr 0
		.amdhsa_user_sgpr_queue_ptr 0
		.amdhsa_user_sgpr_kernarg_segment_ptr 1
		.amdhsa_user_sgpr_dispatch_id 0
		.amdhsa_user_sgpr_kernarg_preload_length 0
		.amdhsa_user_sgpr_kernarg_preload_offset 0
		.amdhsa_user_sgpr_private_segment_size 0
		.amdhsa_uses_dynamic_stack 0
		.amdhsa_enable_private_segment 0
		.amdhsa_system_sgpr_workgroup_id_x 1
		.amdhsa_system_sgpr_workgroup_id_y 0
		.amdhsa_system_sgpr_workgroup_id_z 0
		.amdhsa_system_sgpr_workgroup_info 0
		.amdhsa_system_vgpr_workitem_id 0
		.amdhsa_next_free_vgpr 254
		.amdhsa_next_free_sgpr 96
		.amdhsa_accum_offset 256
		.amdhsa_reserve_vcc 1
		.amdhsa_float_round_mode_32 0
		.amdhsa_float_round_mode_16_64 0
		.amdhsa_float_denorm_mode_32 3
		.amdhsa_float_denorm_mode_16_64 3
		.amdhsa_dx10_clamp 1
		.amdhsa_ieee_mode 1
		.amdhsa_fp16_overflow 0
		.amdhsa_tg_split 0
		.amdhsa_exception_fp_ieee_invalid_op 0
		.amdhsa_exception_fp_denorm_src 0
		.amdhsa_exception_fp_ieee_div_zero 0
		.amdhsa_exception_fp_ieee_overflow 0
		.amdhsa_exception_fp_ieee_underflow 0
		.amdhsa_exception_fp_ieee_inexact 0
		.amdhsa_exception_int_div_zero 0
	.end_amdhsa_kernel
